# adds: DOWN epilogue x16 scale folded into the MFMA block scale (exact), hazard pads after the removals
# baseline (speedup 1.0000x reference)
; #define PG8_STAGE(bufoff, gbase, voff) do { _Pragma("unroll") for (int _i = 0; _i < 2; ++_i) \
;         __builtin_amdgcn_global_load_lds((const unsigned*)((const char*)(gbase) + (voff)[_i]), (PG8_LAS unsigned*)(lds + (bufoff) + ldsw + _i * 8192), 16, 0, 0); } while (0)
; #define PG8_STAGE_A(bufoff, gbase, OA, h) do { _Pragma("unroll") for (int _i = 0; _i < 2; ++_i) \
;         __builtin_amdgcn_global_load_lds((const unsigned*)((const char*)(gbase) + (OA)[h][_i]), (PG8_LAS unsigned*)(lds + (bufoff) + ldsw + _i * 8192), 16, 0, 0); } while (0)
; #define PG8_WAIT_V(n) asm volatile("s_waitcnt vmcnt(" #n ")" ::: "memory")
; #define PG8_WAIT_L(n) asm volatile("s_waitcnt lgkmcnt(" #n ")" ::: "memory")
; #define PG8_BAR __builtin_amdgcn_s_barrier()
; #define PG8_SCHED __builtin_amdgcn_sched_barrier(0)
;     ...
;             PG8_LDB(B0, 0, 0); PG8_LDB(B1, 0, 1); PG8_SCHED; PG8_LDA(At, 0, 0); PG8_STAGE_A(PG8_SA(1, 1), a1, oc, 1);
;             PG8_WAIT_V(8); PG8_WAIT_L(0); PG8_BAR; PG8_MMA(0, 0, At, B0); PG8_MMA(0, 1, At, B1); PG8_BAR; PG8_SCHED;
;             PG8_LDA(At, 0, 1); PG8_STAGE(PG8_SB(0, 0), b2, voffB); PG8_STAGE(PG8_SB(0, 1), b2 + hstep, voffB); PG8_STAGE_A(PG8_SA(0, 0), a2, o2, 0);
;             PG8_WAIT_V(8); PG8_WAIT_L(0); PG8_BAR; PG8_MMA(1, 0, At, B0); PG8_MMA(1, 1, At, B1); PG8_BAR; PG8_SCHED;
.LBB0_1631:
	ds_read_b128 v[24:27], v141
	ds_read_b128 v[28:31], v142
	ds_read_b128 v[56:59], v149
	ds_read_b128 v[60:63], v150
	ds_read_b128 v[158:161], v143
	ds_read_b128 v[162:165], v144
	ds_read_b128 v[166:169], v151
	ds_read_b128 v[170:173], v152
	s_add_u32 s2, s20, 0x8000
	s_addc_u32 s3, s21, 0
	v_lshl_add_u64 v[0:1], s[0:1], 0, v[136:137]
	v_lshl_add_u64 v[0:1], v[0:1], 0, s[92:93]
	s_add_i32 m0, s17, 0xc000
	ds_read_b128 v[4:7], v157
	ds_read_b128 v[8:11], v157 offset:16
	ds_read_b128 v[12:15], v157 offset:2048
	ds_read_b128 v[16:19], v157 offset:2064
	ds_read_b128 v[40:43], v157 offset:4096
	ds_read_b128 v[44:47], v157 offset:4112
	ds_read_b128 v[72:75], v157 offset:6144
	ds_read_b128 v[76:79], v157 offset:6160
	global_load_lds_dwordx4 v[0:1], off
	v_lshl_add_u64 v[0:1], s[0:1], 0, v[130:131]
	v_lshl_add_u64 v[0:1], v[0:1], 0, s[92:93]
	s_add_i32 m0, s17, 0xe000
	s_nop 0
	global_load_lds_dwordx4 v[0:1], off
	s_waitcnt vmcnt(16)
	s_waitcnt lgkmcnt(0)
	s_barrier
	s_setprio 1
	s_waitcnt lgkmcnt(0)
	v_mfma_scale_f32_16x16x128_f8f6f4 v[116:119], v[24:31], v[4:11], 0, v212, v212 op_sel_hi:[0,0,0]
	v_mfma_scale_f32_16x16x128_f8f6f4 v[112:115], v[56:63], v[4:11], 0, v212, v212 op_sel_hi:[0,0,0]
	v_mfma_scale_f32_16x16x128_f8f6f4 v[100:103], v[24:31], v[12:19], 0, v212, v212 op_sel_hi:[0,0,0]
	v_mfma_scale_f32_16x16x128_f8f6f4 v[96:99], v[56:63], v[12:19], 0, v212, v212 op_sel_hi:[0,0,0]
	v_mfma_scale_f32_16x16x128_f8f6f4 v[68:71], v[24:31], v[40:47], 0, v212, v212 op_sel_hi:[0,0,0]
	v_mfma_scale_f32_16x16x128_f8f6f4 v[64:67], v[56:63], v[40:47], 0, v212, v212 op_sel_hi:[0,0,0]
	v_mfma_scale_f32_16x16x128_f8f6f4 v[36:39], v[24:31], v[72:79], 0, v212, v212 op_sel_hi:[0,0,0]
	v_mfma_scale_f32_16x16x128_f8f6f4 v[32:35], v[56:63], v[72:79], 0, v212, v212 op_sel_hi:[0,0,0]
	s_setprio 0
	s_setprio 1
	v_mfma_scale_f32_16x16x128_f8f6f4 v[124:127], v[158:165], v[4:11], 0, v212, v212 op_sel_hi:[0,0,0]
	v_mfma_scale_f32_16x16x128_f8f6f4 v[120:123], v[166:173], v[4:11], 0, v212, v212 op_sel_hi:[0,0,0]
	v_mfma_scale_f32_16x16x128_f8f6f4 v[108:111], v[158:165], v[12:19], 0, v212, v212 op_sel_hi:[0,0,0]
	v_mfma_scale_f32_16x16x128_f8f6f4 v[104:107], v[166:173], v[12:19], 0, v212, v212 op_sel_hi:[0,0,0]
	v_mfma_scale_f32_16x16x128_f8f6f4 v[84:87], v[158:165], v[40:47], 0, v212, v212 op_sel_hi:[0,0,0]
	v_mfma_scale_f32_16x16x128_f8f6f4 v[80:83], v[166:173], v[40:47], 0, v212, v212 op_sel_hi:[0,0,0]
	v_mfma_scale_f32_16x16x128_f8f6f4 v[52:55], v[158:165], v[72:79], 0, v212, v212 op_sel_hi:[0,0,0]
	v_mfma_scale_f32_16x16x128_f8f6f4 v[48:51], v[166:173], v[72:79], 0, v212, v212 op_sel_hi:[0,0,0]
	s_setprio 0
	s_barrier
	v_lshl_add_u64 v[138:139], s[20:21], 0, v[180:181]
	s_add_i32 m0, s17, 0x10000
	ds_read_b128 v[182:185], v157 offset:16384
	ds_read_b128 v[186:189], v157 offset:16400
	ds_read_b128 v[190:193], v157 offset:18432
	ds_read_b128 v[194:197], v157 offset:18448
	ds_read_b128 v[202:205], v157 offset:20480
	ds_read_b128 v[206:209], v157 offset:20496
	ds_read_b128 v[220:223], v157 offset:22528
	ds_read_b128 v[224:227], v157 offset:22544
	global_load_lds_dwordx4 v180, s[20:21]
	v_lshl_add_u64 v[174:175], s[20:21], 0, v[132:133]
	s_add_i32 m0, s17, 0x12000
	s_nop 0
	global_load_lds_dwordx4 v132, s[20:21]
	s_add_i32 m0, s17, 0x14000
	v_lshl_add_u64 v[176:177], s[36:37], 0, v[134:135]
	global_load_lds_dwordx4 v180, s[2:3]
	s_add_i32 m0, s17, 0x16000
	v_lshl_add_u64 v[178:179], s[36:37], 0, v[128:129]
	global_load_lds_dwordx4 v132, s[2:3]
	s_mov_b32 m0, s17
	s_nop 0
	global_load_lds_dwordx4 v134, s[36:37]
	s_add_i32 m0, s17, 0x2000
	s_nop 0
	global_load_lds_dwordx4 v128, s[36:37]
	s_waitcnt vmcnt(16)
	s_waitcnt lgkmcnt(0)
	s_barrier
	s_setprio 1
	s_waitcnt lgkmcnt(0)
	v_mfma_scale_f32_16x16x128_f8f6f4 v[76:79], v[24:31], v[182:189], 0, v212, v212 op_sel_hi:[0,0,0]
	v_mfma_scale_f32_16x16x128_f8f6f4 v[72:75], v[56:63], v[182:189], 0, v212, v212 op_sel_hi:[0,0,0]
	v_mfma_scale_f32_16x16x128_f8f6f4 v[44:47], v[24:31], v[190:197], 0, v212, v212 op_sel_hi:[0,0,0]
	v_mfma_scale_f32_16x16x128_f8f6f4 v[40:43], v[56:63], v[190:197], 0, v212, v212 op_sel_hi:[0,0,0]
	v_mfma_scale_f32_16x16x128_f8f6f4 v[20:23], v[24:31], v[202:209], 0, v212, v212 op_sel_hi:[0,0,0]
	v_mfma_scale_f32_16x16x128_f8f6f4 v[16:19], v[56:63], v[202:209], 0, v212, v212 op_sel_hi:[0,0,0]
	v_mfma_scale_f32_16x16x128_f8f6f4 v[8:11], v[24:31], v[220:227], 0, v212, v212 op_sel_hi:[0,0,0]
	v_mfma_scale_f32_16x16x128_f8f6f4 v[4:7], v[56:63], v[220:227], 0, v212, v212 op_sel_hi:[0,0,0]
	s_setprio 0
	s_setprio 1
	v_mfma_scale_f32_16x16x128_f8f6f4 v[92:95], v[158:165], v[182:189], 0, v212, v212 op_sel_hi:[0,0,0]
	v_mfma_scale_f32_16x16x128_f8f6f4 v[88:91], v[166:173], v[182:189], 0, v212, v212 op_sel_hi:[0,0,0]
	v_mfma_scale_f32_16x16x128_f8f6f4 v[60:63], v[158:165], v[190:197], 0, v212, v212 op_sel_hi:[0,0,0]
	v_mfma_scale_f32_16x16x128_f8f6f4 v[56:59], v[166:173], v[190:197], 0, v212, v212 op_sel_hi:[0,0,0]
	v_mfma_scale_f32_16x16x128_f8f6f4 v[28:31], v[158:165], v[202:209], 0, v212, v212 op_sel_hi:[0,0,0]
	v_mfma_scale_f32_16x16x128_f8f6f4 v[24:27], v[166:173], v[202:209], 0, v212, v212 op_sel_hi:[0,0,0]
	v_mfma_scale_f32_16x16x128_f8f6f4 v[12:15], v[158:165], v[220:227], 0, v212, v212 op_sel_hi:[0,0,0]
	v_mfma_scale_f32_16x16x128_f8f6f4 v[0:3], v[166:173], v[220:227], 0, v212, v212 op_sel_hi:[0,0,0]
	s_setprio 0
	s_barrier
; #define PG8_STAGE(bufoff, gbase, voff) do { _Pragma("unroll") for (int _i = 0; _i < 2; ++_i) \
;         __builtin_amdgcn_global_load_lds((const unsigned*)((const char*)(gbase) + (voff)[_i]), (PG8_LAS unsigned*)(lds + (bufoff) + ldsw + _i * 8192), 16, 0, 0); } while (0)
; #define PG8_STAGE_A(bufoff, gbase, OA, h) do { _Pragma("unroll") for (int _i = 0; _i < 2; ++_i) \
;         __builtin_amdgcn_global_load_lds((const unsigned*)((const char*)(gbase) + (OA)[h][_i]), (PG8_LAS unsigned*)(lds + (bufoff) + ldsw + _i * 8192), 16, 0, 0); } while (0)
; #define PG8_WAIT_V(n) asm volatile("s_waitcnt vmcnt(" #n ")" ::: "memory")
; #define PG8_WAIT_L(n) asm volatile("s_waitcnt lgkmcnt(" #n ")" ::: "memory")
; #define PG8_BAR __builtin_amdgcn_s_barrier()
; #define PG8_SCHED __builtin_amdgcn_sched_barrier(0)
;     ...
;             PG8_LDB(B0, 1, 0); PG8_LDB(B1, 1, 1); PG8_SCHED; PG8_LDA(At, 1, 0); PG8_STAGE_A(PG8_SA(0, 1), a2, o2, 1);
;             PG8_WAIT_V(8); PG8_WAIT_L(0); PG8_BAR; PG8_MMA(0, 0, At, B0); PG8_MMA(0, 1, At, B1); PG8_BAR; PG8_SCHED;
;             PG8_LDA(At, 1, 1); PG8_STAGE(PG8_SB(1, 0), b3, voffB); PG8_STAGE(PG8_SB(1, 1), b3 + hstep, voffB); PG8_STAGE_A(PG8_SA(1, 0), a3, o2, 0);
;             PG8_WAIT_V(8); PG8_WAIT_L(0); PG8_BAR; PG8_MMA(1, 0, At, B0); PG8_MMA(1, 1, At, B1); PG8_BAR; PG8_SCHED;
	ds_read_b128 v[158:161], v145
	ds_read_b128 v[162:165], v146
	ds_read_b128 v[166:169], v153
	ds_read_b128 v[170:173], v154
	ds_read_b128 v[182:185], v147
	ds_read_b128 v[186:189], v148
	ds_read_b128 v[190:193], v155
	ds_read_b128 v[194:197], v156
	s_add_i32 m0, s17, 0x4000
	ds_read_b128 v[202:205], v157 offset:32768
	ds_read_b128 v[206:209], v157 offset:32784
	ds_read_b128 v[220:223], v157 offset:34816
	ds_read_b128 v[224:227], v157 offset:34832
	ds_read_b128 v[236:239], v157 offset:36864
	ds_read_b128 v[240:243], v157 offset:36880
	ds_read_b128 v[244:247], v157 offset:38912
	ds_read_b128 v[248:251], v157 offset:38928
	global_load_lds_dwordx4 v136, s[36:37]
	s_add_i32 m0, s17, 0x6000
	s_nop 0
	global_load_lds_dwordx4 v130, s[36:37]
	s_waitcnt vmcnt(8)
	s_waitcnt lgkmcnt(0)
	s_barrier
	s_setprio 1
	s_waitcnt lgkmcnt(0)
	v_mfma_scale_f32_16x16x128_f8f6f4 v[116:119], v[158:165], v[202:209], v[116:119], v212, v212 op_sel_hi:[0,0,0]
	v_mfma_scale_f32_16x16x128_f8f6f4 v[112:115], v[166:173], v[202:209], v[112:115], v212, v212 op_sel_hi:[0,0,0]
	v_mfma_scale_f32_16x16x128_f8f6f4 v[100:103], v[158:165], v[220:227], v[100:103], v212, v212 op_sel_hi:[0,0,0]
	v_mfma_scale_f32_16x16x128_f8f6f4 v[96:99], v[166:173], v[220:227], v[96:99], v212, v212 op_sel_hi:[0,0,0]
	v_mfma_scale_f32_16x16x128_f8f6f4 v[68:71], v[158:165], v[236:243], v[68:71], v212, v212 op_sel_hi:[0,0,0]
	v_mfma_scale_f32_16x16x128_f8f6f4 v[64:67], v[166:173], v[236:243], v[64:67], v212, v212 op_sel_hi:[0,0,0]
	v_mfma_scale_f32_16x16x128_f8f6f4 v[36:39], v[158:165], v[244:251], v[36:39], v212, v212 op_sel_hi:[0,0,0]
	v_mfma_scale_f32_16x16x128_f8f6f4 v[32:35], v[166:173], v[244:251], v[32:35], v212, v212 op_sel_hi:[0,0,0]
	s_setprio 0
	s_setprio 1
	v_mfma_scale_f32_16x16x128_f8f6f4 v[124:127], v[182:189], v[202:209], v[124:127], v212, v212 op_sel_hi:[0,0,0]
	v_mfma_scale_f32_16x16x128_f8f6f4 v[120:123], v[190:197], v[202:209], v[120:123], v212, v212 op_sel_hi:[0,0,0]
	v_mfma_scale_f32_16x16x128_f8f6f4 v[108:111], v[182:189], v[220:227], v[108:111], v212, v212 op_sel_hi:[0,0,0]
	v_mfma_scale_f32_16x16x128_f8f6f4 v[104:107], v[190:197], v[220:227], v[104:107], v212, v212 op_sel_hi:[0,0,0]
	v_mfma_scale_f32_16x16x128_f8f6f4 v[84:87], v[182:189], v[236:243], v[84:87], v212, v212 op_sel_hi:[0,0,0]
	v_mfma_scale_f32_16x16x128_f8f6f4 v[80:83], v[190:197], v[236:243], v[80:83], v212, v212 op_sel_hi:[0,0,0]
	v_mfma_scale_f32_16x16x128_f8f6f4 v[52:55], v[182:189], v[244:251], v[52:55], v212, v212 op_sel_hi:[0,0,0]
	v_mfma_scale_f32_16x16x128_f8f6f4 v[48:51], v[190:197], v[244:251], v[48:51], v212, v212 op_sel_hi:[0,0,0]
	s_setprio 0
	s_barrier
	s_mov_b32 m0, s18
	v_lshl_add_u64 v[138:139], v[138:139], 0, s[92:93]
	s_add_u32 s0, s20, 0x8080
	ds_read_b128 v[202:205], v157 offset:49152
	ds_read_b128 v[206:209], v157 offset:49168
	ds_read_b128 v[220:223], v157 offset:51200
	ds_read_b128 v[224:227], v157 offset:51216
	ds_read_b128 v[236:239], v157 offset:53248
	ds_read_b128 v[240:243], v157 offset:53264
	ds_read_b128 v[244:247], v157 offset:55296
	ds_read_b128 v[248:251], v157 offset:55312
	global_load_lds_dwordx4 v[138:139], off
	v_lshl_add_u64 v[138:139], v[174:175], 0, s[92:93]
	s_mov_b32 m0, s19
	s_addc_u32 s1, s21, 0
	global_load_lds_dwordx4 v[138:139], off
	s_mov_b32 m0, s38
	s_nop 0
	global_load_lds_dwordx4 v180, s[0:1]
	s_mov_b32 m0, s39
	s_nop 0
	global_load_lds_dwordx4 v132, s[0:1]
	v_lshl_add_u64 v[138:139], v[176:177], 0, s[92:93]
	s_mov_b32 m0, s28
	s_nop 0
	global_load_lds_dwordx4 v[138:139], off
	v_lshl_add_u64 v[138:139], v[178:179], 0, s[92:93]
	s_mov_b32 m0, s29
	s_nop 0
	global_load_lds_dwordx4 v[138:139], off
	s_waitcnt vmcnt(8)
	s_waitcnt lgkmcnt(0)
	s_barrier
	s_setprio 1
	s_waitcnt lgkmcnt(0)
	v_mfma_scale_f32_16x16x128_f8f6f4 v[76:79], v[158:165], v[202:209], v[76:79], v212, v212 op_sel_hi:[0,0,0]
	v_mfma_scale_f32_16x16x128_f8f6f4 v[72:75], v[166:173], v[202:209], v[72:75], v212, v212 op_sel_hi:[0,0,0]
	v_mfma_scale_f32_16x16x128_f8f6f4 v[44:47], v[158:165], v[220:227], v[44:47], v212, v212 op_sel_hi:[0,0,0]
	v_mfma_scale_f32_16x16x128_f8f6f4 v[40:43], v[166:173], v[220:227], v[40:43], v212, v212 op_sel_hi:[0,0,0]
	v_mfma_scale_f32_16x16x128_f8f6f4 v[20:23], v[158:165], v[236:243], v[20:23], v212, v212 op_sel_hi:[0,0,0]
	v_mfma_scale_f32_16x16x128_f8f6f4 v[16:19], v[166:173], v[236:243], v[16:19], v212, v212 op_sel_hi:[0,0,0]
	v_mfma_scale_f32_16x16x128_f8f6f4 v[8:11], v[158:165], v[244:251], v[8:11], v212, v212 op_sel_hi:[0,0,0]
	v_mfma_scale_f32_16x16x128_f8f6f4 v[4:7], v[166:173], v[244:251], v[4:7], v212, v212 op_sel_hi:[0,0,0]
	s_setprio 0
	s_setprio 1
	v_mfma_scale_f32_16x16x128_f8f6f4 v[92:95], v[182:189], v[202:209], v[92:95], v212, v212 op_sel_hi:[0,0,0]
	v_mfma_scale_f32_16x16x128_f8f6f4 v[88:91], v[190:197], v[202:209], v[88:91], v212, v212 op_sel_hi:[0,0,0]
	v_mfma_scale_f32_16x16x128_f8f6f4 v[60:63], v[182:189], v[220:227], v[60:63], v212, v212 op_sel_hi:[0,0,0]
	v_mfma_scale_f32_16x16x128_f8f6f4 v[56:59], v[190:197], v[220:227], v[56:59], v212, v212 op_sel_hi:[0,0,0]
	v_mfma_scale_f32_16x16x128_f8f6f4 v[28:31], v[182:189], v[236:243], v[28:31], v212, v212 op_sel_hi:[0,0,0]
	v_mfma_scale_f32_16x16x128_f8f6f4 v[24:27], v[190:197], v[236:243], v[24:27], v212, v212 op_sel_hi:[0,0,0]
	v_mfma_scale_f32_16x16x128_f8f6f4 v[12:15], v[182:189], v[244:251], v[12:15], v212, v212 op_sel_hi:[0,0,0]
	v_mfma_scale_f32_16x16x128_f8f6f4 v[0:3], v[190:197], v[244:251], v[0:3], v212, v212 op_sel_hi:[0,0,0]
	s_setprio 0
	s_barrier
; __device__ __forceinline__ unsigned pk4f8(float a, float b, float c, float d) { int w = 0; w = __builtin_amdgcn_cvt_pk_fp8_f32(a, b, w, false); w = __builtin_amdgcn_cvt_pk_fp8_f32(c, d, w, true); return (unsigned)w; }
;     __device__ __forceinline__ void operator()(const f32x4 (&acc)[2][2][4][2], const Unit& u, int wr, int wc, int fr, int fq) const {
;         unsigned char* base = O; int pm = u.pm; int ld = ldc; if (pm >= pm_split) { base = O2; pm -= pm_off2; ld = ldc2; }
;         const int row0 = pm * BM + wr * 64 + fr; const int col0 = u.pn * BM + wc * 32 + ((fq & 1) ? HALF + 8 * (fq - 1) : 8 * fq);
; #pragma unroll
;         for (int ai = 0; ai < 2; ++ai)
; #pragma unroll
;             for (int m = 0; m < 4; ++m) { unsigned char* rowp = base + (size_t)(row0 + ai * HALF + m * 16) * ld + col0;
;                 const f32x4 p0 = acc[ai][0][m][0] * scale, p1 = acc[ai][0][m][1] * scale, q0 = acc[ai][1][m][0] * scale, q1 = acc[ai][1][m][1] * scale;
;                 unsigned ax = pk4f8(p0[0], p0[1], p0[2], p0[3]), ay = pk4f8(p1[0], p1[1], p1[2], p1[3]), bx = pk4f8(q0[0], q0[1], q0[2], q0[3]), by = pk4f8(q1[0], q1[1], q1[2], q1[3]);
;                 { auto r = __builtin_amdgcn_permlane16_swap(ax, bx, false, false); ax = r[0]; bx = r[1]; }
;                 { auto r = __builtin_amdgcn_permlane16_swap(ay, by, false, false); ay = r[0]; by = r[1]; }
;                 u32x4 w; w.x = ax; w.y = ay; w.z = bx; w.w = by;
;                 *(u32x4*)rowp = w; }
	s_cmpk_lt_i32 s41, 0x480
	v_mov_b32_e32 v139, v200
	s_cselect_b32 s0, 0, 0xfffffb80
	s_mov_b32 s1, 0x18c00000
	s_cselect_b32 s1, s1, 0x2ae00000
	s_add_i32 s2, s0, s41
	v_ashrrev_i32_e32 v158, 1, v139
	s_add_u32 s0, s6, s1
	v_and_b32_e32 v138, 16, v139
	v_and_b32_e32 v158, -8, v158
	s_addc_u32 s1, s7, 0
	s_lshl_b32 s3, s42, 8
	v_add_u32_e32 v159, 0x78, v158
	v_cmp_eq_u32_e32 vcc, 0, v138
	v_and_or_b32 v139, v139, 15, v140
	s_or_b32 s3, s3, s16
	v_cndmask_b32_e32 v138, v159, v158, vcc
	v_lshl_add_u32 v158, s2, 8, v139
	s_mov_b32 s2, 0x41800000
	v_mov_b64_e32 v[162:163], v[114:115]
	v_mov_b64_e32 v[114:115], v[112:113]
	v_cvt_pk_fp8_f32 v113, v114, v115
	v_cvt_pk_fp8_f32 v112, v116, v117
	v_cvt_pk_fp8_f32 v114, v124, v125
	v_cvt_pk_fp8_f32 v115, v120, v121
	v_cvt_pk_fp8_f32 v112, v118, v119 op_sel:[0,0,1]
	v_cvt_pk_fp8_f32 v114, v126, v127 op_sel:[0,0,1]
	v_cvt_pk_fp8_f32 v113, v162, v163 op_sel:[0,0,1]
	v_cvt_pk_fp8_f32 v115, v122, v123 op_sel:[0,0,1]
	v_add_u32_e32 v138, s3, v138
	v_ashrrev_i32_e32 v139, 31, v138
	v_ashrrev_i32_e32 v159, 31, v158
	v_lshl_add_u64 v[160:161], s[0:1], 0, v[138:139]
	v_lshlrev_b64 v[138:139], 10, v[158:159]
	v_lshl_add_u64 v[138:139], v[160:161], 0, v[138:139]
	v_permlane16_swap_b32_e32 v112, v114
	v_permlane16_swap_b32_e32 v113, v115
	global_store_dwordx4 v[138:139], v[112:115], off
	s_nop 1
	v_mov_b64_e32 v[114:115], v[98:99]
	v_mov_b64_e32 v[98:99], v[96:97]
	v_cvt_pk_fp8_f32 v97, v98, v99
	v_cvt_pk_fp8_f32 v96, v100, v101
	v_cvt_pk_fp8_f32 v98, v108, v109
	v_cvt_pk_fp8_f32 v99, v104, v105
	v_cvt_pk_fp8_f32 v96, v102, v103 op_sel:[0,0,1]
	v_cvt_pk_fp8_f32 v98, v110, v111 op_sel:[0,0,1]
	v_cvt_pk_fp8_f32 v97, v114, v115 op_sel:[0,0,1]
	v_cvt_pk_fp8_f32 v99, v106, v107 op_sel:[0,0,1]
	v_or_b32_e32 v112, 16, v158
	v_ashrrev_i32_e32 v113, 31, v112
	v_lshlrev_b64 v[112:113], 10, v[112:113]
	v_lshl_add_u64 v[112:113], v[160:161], 0, v[112:113]
	v_permlane16_swap_b32_e32 v96, v98
	v_permlane16_swap_b32_e32 v97, v99
	global_store_dwordx4 v[112:113], v[96:99], off
	s_nop 1
	v_mov_b64_e32 v[98:99], v[66:67]
	v_mov_b64_e32 v[66:67], v[64:65]
	v_cvt_pk_fp8_f32 v65, v66, v67
	v_cvt_pk_fp8_f32 v64, v68, v69
	v_cvt_pk_fp8_f32 v66, v84, v85
	v_cvt_pk_fp8_f32 v67, v80, v81
	v_cvt_pk_fp8_f32 v64, v70, v71 op_sel:[0,0,1]
	v_cvt_pk_fp8_f32 v66, v86, v87 op_sel:[0,0,1]
	v_cvt_pk_fp8_f32 v65, v98, v99 op_sel:[0,0,1]
	v_cvt_pk_fp8_f32 v67, v82, v83 op_sel:[0,0,1]
	v_or_b32_e32 v96, 32, v158
	v_ashrrev_i32_e32 v97, 31, v96
	v_lshlrev_b64 v[96:97], 10, v[96:97]
	v_lshl_add_u64 v[96:97], v[160:161], 0, v[96:97]
	v_permlane16_swap_b32_e32 v64, v66
	v_permlane16_swap_b32_e32 v65, v67
	global_store_dwordx4 v[96:97], v[64:67], off
	s_nop 1
	v_mov_b64_e32 v[66:67], v[34:35]
	v_mov_b64_e32 v[34:35], v[32:33]
	v_cvt_pk_fp8_f32 v33, v34, v35
	v_cvt_pk_fp8_f32 v32, v36, v37
	v_cvt_pk_fp8_f32 v34, v52, v53
	v_cvt_pk_fp8_f32 v35, v48, v49
	v_cvt_pk_fp8_f32 v32, v38, v39 op_sel:[0,0,1]
	v_cvt_pk_fp8_f32 v34, v54, v55 op_sel:[0,0,1]
	v_cvt_pk_fp8_f32 v33, v66, v67 op_sel:[0,0,1]
	v_cvt_pk_fp8_f32 v35, v50, v51 op_sel:[0,0,1]
	v_or_b32_e32 v64, 48, v158
	v_ashrrev_i32_e32 v65, 31, v64
	v_lshlrev_b64 v[64:65], 10, v[64:65]
	v_lshl_add_u64 v[64:65], v[160:161], 0, v[64:65]
	v_permlane16_swap_b32_e32 v32, v34
	v_permlane16_swap_b32_e32 v33, v35
	global_store_dwordx4 v[64:65], v[32:35], off
	s_nop 1
	v_mov_b64_e32 v[48:49], v[72:73]
	v_mov_b64_e32 v[52:53], v[92:93]
	v_mov_b64_e32 v[34:35], v[76:77]
	v_mov_b64_e32 v[64:65], v[88:89]
	v_cvt_pk_fp8_f32 v32, v34, v35
	v_cvt_pk_fp8_f32 v33, v48, v49
	v_cvt_pk_fp8_f32 v34, v52, v53
	v_cvt_pk_fp8_f32 v35, v64, v65
	v_mov_b64_e32 v[36:37], v[78:79]
	v_mov_b64_e32 v[38:39], v[74:75]
	v_mov_b64_e32 v[50:51], v[94:95]
	v_mov_b64_e32 v[54:55], v[90:91]
	v_cvt_pk_fp8_f32 v32, v36, v37 op_sel:[0,0,1]
	v_cvt_pk_fp8_f32 v34, v50, v51 op_sel:[0,0,1]
	v_cvt_pk_fp8_f32 v33, v38, v39 op_sel:[0,0,1]
	v_cvt_pk_fp8_f32 v35, v54, v55 op_sel:[0,0,1]
	s_mov_b32 s0, 0x20000
	v_add_co_u32_e32 v36, vcc, s0, v138
	v_permlane16_swap_b32_e32 v32, v34
	v_permlane16_swap_b32_e32 v33, v35
	v_addc_co_u32_e32 v37, vcc, 0, v139, vcc
	global_store_dwordx4 v[36:37], v[32:35], off
	s_nop 1
	v_mov_b64_e32 v[48:49], v[56:57]
	v_mov_b64_e32 v[34:35], v[44:45]
	v_mov_b64_e32 v[44:45], v[60:61]
	v_cvt_pk_fp8_f32 v32, v34, v35
	v_cvt_pk_fp8_f32 v33, v40, v41
	v_cvt_pk_fp8_f32 v34, v44, v45
	v_cvt_pk_fp8_f32 v35, v48, v49
	v_mov_b64_e32 v[36:37], v[46:47]
	v_mov_b64_e32 v[38:39], v[42:43]
	v_mov_b64_e32 v[42:43], v[62:63]
	v_mov_b64_e32 v[46:47], v[58:59]
	v_cvt_pk_fp8_f32 v32, v36, v37 op_sel:[0,0,1]
	v_cvt_pk_fp8_f32 v34, v42, v43 op_sel:[0,0,1]
	v_cvt_pk_fp8_f32 v33, v38, v39 op_sel:[0,0,1]
	v_cvt_pk_fp8_f32 v35, v46, v47 op_sel:[0,0,1]
	s_mov_b32 s0, 0x24000
	v_add_co_u32_e32 v36, vcc, s0, v138
	v_permlane16_swap_b32_e32 v32, v34
	v_permlane16_swap_b32_e32 v33, v35
	v_addc_co_u32_e32 v37, vcc, 0, v139, vcc
	global_store_dwordx4 v[36:37], v[32:35], off
	s_nop 1
	v_mov_b64_e32 v[32:33], v[18:19]
	v_mov_b64_e32 v[18:19], v[16:17]
	v_cvt_pk_fp8_f32 v17, v18, v19
	v_cvt_pk_fp8_f32 v16, v20, v21
	v_cvt_pk_fp8_f32 v18, v28, v29
	v_cvt_pk_fp8_f32 v19, v24, v25
	v_cvt_pk_fp8_f32 v16, v22, v23 op_sel:[0,0,1]
	v_cvt_pk_fp8_f32 v18, v30, v31 op_sel:[0,0,1]
	v_cvt_pk_fp8_f32 v17, v32, v33 op_sel:[0,0,1]
	v_cvt_pk_fp8_f32 v19, v26, v27 op_sel:[0,0,1]
	s_mov_b32 s0, 0x28000
	v_add_co_u32_e32 v20, vcc, s0, v138
	v_permlane16_swap_b32_e32 v16, v18
	v_permlane16_swap_b32_e32 v17, v19
	v_addc_co_u32_e32 v21, vcc, 0, v139, vcc
	global_store_dwordx4 v[20:21], v[16:19], off
	s_nop 1
	v_mov_b64_e32 v[16:17], v[2:3]
	v_mov_b64_e32 v[18:19], v[0:1]
	v_cvt_pk_fp8_f32 v0, v8, v9
	v_cvt_pk_fp8_f32 v1, v4, v5
	v_cvt_pk_fp8_f32 v2, v12, v13
	v_cvt_pk_fp8_f32 v3, v18, v19
	v_cvt_pk_fp8_f32 v0, v10, v11 op_sel:[0,0,1]
	v_cvt_pk_fp8_f32 v2, v14, v15 op_sel:[0,0,1]
	v_cvt_pk_fp8_f32 v1, v6, v7 op_sel:[0,0,1]
	v_cvt_pk_fp8_f32 v3, v16, v17 op_sel:[0,0,1]
	v_add_co_u32_e32 v4, vcc, 0x2c000, v138
	v_permlane16_swap_b32_e32 v0, v2
	s_nop 0
	v_addc_co_u32_e32 v5, vcc, 0, v139, vcc
	v_permlane16_swap_b32_e32 v1, v3
	s_add_i32 s40, s40, 1
	s_andn2_b64 vcc, exec, s[26:27]
	s_mov_b32 s42, s22
	s_mov_b32 s41, s14
	s_mov_b64 s[0:1], s[36:37]
	global_store_dwordx4 v[4:5], v[0:3], off
	s_nop 1
	s_cbranch_vccz .LBB0_1638
